# P6 router MFMA loop unrolled into 8 half-trips with three operand buffers (loads two half-trips ahead), same MFMA order
# speedup vs baseline: 1.0045x; 1.0019x over previous
.LBB0_711:
	v_lshl_add_u64 v[52:53], v[50:51], 0, s[12:13]
	v_add_co_u32_e32 v152, vcc, s42, v52
	v_lshl_add_u64 v[54:55], v[48:49], 0, s[12:13]
	s_nop 0
	v_addc_co_u32_e32 v153, vcc, 0, v53, vcc
	v_add_co_u32_e32 v154, vcc, s45, v52
	s_nop 0
	s_nop 0
	v_addc_co_u32_e32 v155, vcc, 0, v53, vcc
	v_add_co_u32_e32 v156, vcc, s46, v54
	s_nop 0
	s_nop 0
	v_addc_co_u32_e32 v157, vcc, 0, v55, vcc
	v_add_co_u32_e32 v158, vcc, s47, v54
	s_nop 0
	s_nop 0
	v_addc_co_u32_e32 v159, vcc, 0, v55, vcc
	global_load_dwordx4 v[176:179], v[152:153], off
	global_load_dwordx4 v[180:183], v[156:157], off
	global_load_dwordx4 v[184:187], v[154:155], off
	global_load_dwordx4 v[188:191], v[158:159], off
	global_load_dwordx4 v[192:195], v[152:153], off offset:32
	global_load_dwordx4 v[196:199], v[156:157], off offset:32
	global_load_dwordx4 v[200:203], v[154:155], off offset:32
	global_load_dwordx4 v[204:207], v[158:159], off offset:32
	global_load_dwordx4 v[208:211], v[152:153], off offset:64
	global_load_dwordx4 v[212:215], v[156:157], off offset:64
	global_load_dwordx4 v[216:219], v[154:155], off offset:64
	global_load_dwordx4 v[220:223], v[158:159], off offset:64
	global_load_dwordx4 v[224:227], v[152:153], off offset:96
	global_load_dwordx4 v[228:231], v[156:157], off offset:96
	global_load_dwordx4 v[232:235], v[154:155], off offset:96
	global_load_dwordx4 v[236:239], v[158:159], off offset:96
	global_load_dwordx4 v[240:243], v[152:153], off offset:128
	global_load_dwordx4 v[244:247], v[156:157], off offset:128
	global_load_dwordx4 v[248:251], v[154:155], off offset:128
	global_load_dwordx4 v[52:55], v[158:159], off offset:128
	global_load_dwordx4 v[56:59], v[152:153], off offset:160
	global_load_dwordx4 v[60:63], v[156:157], off offset:160
	global_load_dwordx4 v[64:67], v[154:155], off offset:160
	global_load_dwordx4 v[68:71], v[158:159], off offset:160
	s_waitcnt vmcnt(16)
	v_mfma_f32_32x32x16_bf16 v[2:17], v[176:179], v[180:183], v[2:17]
	v_mfma_f32_32x32x16_bf16 v[18:33], v[184:187], v[180:183], v[18:33]
	v_mfma_f32_32x32x16_bf16 v[2:17], v[176:179], v[188:191], v[2:17]
	v_mfma_f32_32x32x16_bf16 v[18:33], v[184:187], v[188:191], v[18:33]
	v_mfma_f32_32x32x16_bf16 v[2:17], v[192:195], v[196:199], v[2:17]
	v_mfma_f32_32x32x16_bf16 v[18:33], v[200:203], v[196:199], v[18:33]
	v_mfma_f32_32x32x16_bf16 v[2:17], v[192:195], v[204:207], v[2:17]
	v_mfma_f32_32x32x16_bf16 v[18:33], v[200:203], v[204:207], v[18:33]
	global_load_dwordx4 v[176:179], v[152:153], off offset:192
	global_load_dwordx4 v[180:183], v[156:157], off offset:192
	global_load_dwordx4 v[184:187], v[154:155], off offset:192
	global_load_dwordx4 v[188:191], v[158:159], off offset:192
	global_load_dwordx4 v[192:195], v[152:153], off offset:224
	global_load_dwordx4 v[196:199], v[156:157], off offset:224
	global_load_dwordx4 v[200:203], v[154:155], off offset:224
	global_load_dwordx4 v[204:207], v[158:159], off offset:224
	s_waitcnt vmcnt(16)
	v_mfma_f32_32x32x16_bf16 v[2:17], v[208:211], v[212:215], v[2:17]
	v_mfma_f32_32x32x16_bf16 v[18:33], v[216:219], v[212:215], v[18:33]
	v_mfma_f32_32x32x16_bf16 v[2:17], v[208:211], v[220:223], v[2:17]
	v_mfma_f32_32x32x16_bf16 v[18:33], v[216:219], v[220:223], v[18:33]
	v_mfma_f32_32x32x16_bf16 v[2:17], v[224:227], v[228:231], v[2:17]
	v_mfma_f32_32x32x16_bf16 v[18:33], v[232:235], v[228:231], v[18:33]
	v_mfma_f32_32x32x16_bf16 v[2:17], v[224:227], v[236:239], v[2:17]
	v_mfma_f32_32x32x16_bf16 v[18:33], v[232:235], v[236:239], v[18:33]
	global_load_dwordx4 v[208:211], v[152:153], off offset:256
	global_load_dwordx4 v[212:215], v[156:157], off offset:256
	global_load_dwordx4 v[216:219], v[154:155], off offset:256
	global_load_dwordx4 v[220:223], v[158:159], off offset:256
	global_load_dwordx4 v[224:227], v[152:153], off offset:288
	global_load_dwordx4 v[228:231], v[156:157], off offset:288
	global_load_dwordx4 v[232:235], v[154:155], off offset:288
	global_load_dwordx4 v[236:239], v[158:159], off offset:288
	s_waitcnt vmcnt(16)
	v_mfma_f32_32x32x16_bf16 v[2:17], v[240:243], v[244:247], v[2:17]
	v_mfma_f32_32x32x16_bf16 v[18:33], v[248:251], v[244:247], v[18:33]
	v_mfma_f32_32x32x16_bf16 v[2:17], v[240:243], v[52:55], v[2:17]
	v_mfma_f32_32x32x16_bf16 v[18:33], v[248:251], v[52:55], v[18:33]
	v_mfma_f32_32x32x16_bf16 v[2:17], v[56:59], v[60:63], v[2:17]
	v_mfma_f32_32x32x16_bf16 v[18:33], v[64:67], v[60:63], v[18:33]
	v_mfma_f32_32x32x16_bf16 v[2:17], v[56:59], v[68:71], v[2:17]
	v_mfma_f32_32x32x16_bf16 v[18:33], v[64:67], v[68:71], v[18:33]
	global_load_dwordx4 v[240:243], v[152:153], off offset:320
	global_load_dwordx4 v[244:247], v[156:157], off offset:320
	global_load_dwordx4 v[248:251], v[154:155], off offset:320
	global_load_dwordx4 v[52:55], v[158:159], off offset:320
	global_load_dwordx4 v[56:59], v[152:153], off offset:352
	global_load_dwordx4 v[60:63], v[156:157], off offset:352
	global_load_dwordx4 v[64:67], v[154:155], off offset:352
	global_load_dwordx4 v[68:71], v[158:159], off offset:352
	s_waitcnt vmcnt(16)
	v_mfma_f32_32x32x16_bf16 v[2:17], v[176:179], v[180:183], v[2:17]
	v_mfma_f32_32x32x16_bf16 v[18:33], v[184:187], v[180:183], v[18:33]
	v_mfma_f32_32x32x16_bf16 v[2:17], v[176:179], v[188:191], v[2:17]
	v_mfma_f32_32x32x16_bf16 v[18:33], v[184:187], v[188:191], v[18:33]
	v_mfma_f32_32x32x16_bf16 v[2:17], v[192:195], v[196:199], v[2:17]
	v_mfma_f32_32x32x16_bf16 v[18:33], v[200:203], v[196:199], v[18:33]
	v_mfma_f32_32x32x16_bf16 v[2:17], v[192:195], v[204:207], v[2:17]
	v_mfma_f32_32x32x16_bf16 v[18:33], v[200:203], v[204:207], v[18:33]
	global_load_dwordx4 v[176:179], v[152:153], off offset:384
	global_load_dwordx4 v[180:183], v[156:157], off offset:384
	global_load_dwordx4 v[184:187], v[154:155], off offset:384
	global_load_dwordx4 v[188:191], v[158:159], off offset:384
	global_load_dwordx4 v[192:195], v[152:153], off offset:416
	global_load_dwordx4 v[196:199], v[156:157], off offset:416
	global_load_dwordx4 v[200:203], v[154:155], off offset:416
	global_load_dwordx4 v[204:207], v[158:159], off offset:416
	s_waitcnt vmcnt(16)
	v_mfma_f32_32x32x16_bf16 v[2:17], v[208:211], v[212:215], v[2:17]
	v_mfma_f32_32x32x16_bf16 v[18:33], v[216:219], v[212:215], v[18:33]
	v_mfma_f32_32x32x16_bf16 v[2:17], v[208:211], v[220:223], v[2:17]
	v_mfma_f32_32x32x16_bf16 v[18:33], v[216:219], v[220:223], v[18:33]
	v_mfma_f32_32x32x16_bf16 v[2:17], v[224:227], v[228:231], v[2:17]
	v_mfma_f32_32x32x16_bf16 v[18:33], v[232:235], v[228:231], v[18:33]
	v_mfma_f32_32x32x16_bf16 v[2:17], v[224:227], v[236:239], v[2:17]
	v_mfma_f32_32x32x16_bf16 v[18:33], v[232:235], v[236:239], v[18:33]
	global_load_dwordx4 v[208:211], v[152:153], off offset:448
	global_load_dwordx4 v[212:215], v[156:157], off offset:448
	global_load_dwordx4 v[216:219], v[154:155], off offset:448
	global_load_dwordx4 v[220:223], v[158:159], off offset:448
	global_load_dwordx4 v[224:227], v[152:153], off offset:480
	global_load_dwordx4 v[228:231], v[156:157], off offset:480
	global_load_dwordx4 v[232:235], v[154:155], off offset:480
	global_load_dwordx4 v[236:239], v[158:159], off offset:480
	s_waitcnt vmcnt(16)
	v_mfma_f32_32x32x16_bf16 v[2:17], v[240:243], v[244:247], v[2:17]
	v_mfma_f32_32x32x16_bf16 v[18:33], v[248:251], v[244:247], v[18:33]
	v_mfma_f32_32x32x16_bf16 v[2:17], v[240:243], v[52:55], v[2:17]
	v_mfma_f32_32x32x16_bf16 v[18:33], v[248:251], v[52:55], v[18:33]
	v_mfma_f32_32x32x16_bf16 v[2:17], v[56:59], v[60:63], v[2:17]
	v_mfma_f32_32x32x16_bf16 v[18:33], v[64:67], v[60:63], v[18:33]
	v_mfma_f32_32x32x16_bf16 v[2:17], v[56:59], v[68:71], v[2:17]
	v_mfma_f32_32x32x16_bf16 v[18:33], v[64:67], v[68:71], v[18:33]
	s_waitcnt vmcnt(8)
	v_mfma_f32_32x32x16_bf16 v[2:17], v[176:179], v[180:183], v[2:17]
	v_mfma_f32_32x32x16_bf16 v[18:33], v[184:187], v[180:183], v[18:33]
	v_mfma_f32_32x32x16_bf16 v[2:17], v[176:179], v[188:191], v[2:17]
	v_mfma_f32_32x32x16_bf16 v[18:33], v[184:187], v[188:191], v[18:33]
	v_mfma_f32_32x32x16_bf16 v[2:17], v[192:195], v[196:199], v[2:17]
	v_mfma_f32_32x32x16_bf16 v[18:33], v[200:203], v[196:199], v[18:33]
	v_mfma_f32_32x32x16_bf16 v[2:17], v[192:195], v[204:207], v[2:17]
	v_mfma_f32_32x32x16_bf16 v[18:33], v[200:203], v[204:207], v[18:33]
	s_waitcnt vmcnt(0)
	v_mfma_f32_32x32x16_bf16 v[2:17], v[208:211], v[212:215], v[2:17]
	v_mfma_f32_32x32x16_bf16 v[18:33], v[216:219], v[212:215], v[18:33]
	v_mfma_f32_32x32x16_bf16 v[2:17], v[208:211], v[220:223], v[2:17]
	v_mfma_f32_32x32x16_bf16 v[18:33], v[216:219], v[220:223], v[18:33]
	v_mfma_f32_32x32x16_bf16 v[2:17], v[224:227], v[228:231], v[2:17]
	v_mfma_f32_32x32x16_bf16 v[18:33], v[232:235], v[228:231], v[18:33]
	v_mfma_f32_32x32x16_bf16 v[2:17], v[224:227], v[236:239], v[2:17]
	v_mfma_f32_32x32x16_bf16 v[18:33], v[232:235], v[236:239], v[18:33]
	s_movk_i32 s12, 0x200
	s_mov_b32 s13, 0
	s_cmpk_eq_i32 s12, 0x200
	s_nop 9
	ds_write2_b32 v74, v2, v3 offset1:32
	v_add_u32_e32 v2, 0x1000, v74
	ds_write2_b32 v2, v18, v19 offset1:32
	ds_write2_b32 v74, v4, v5 offset0:64 offset1:96
	ds_write2_b32 v2, v20, v21 offset0:64 offset1:96
	v_add_u32_e32 v2, 0x400, v74
	v_add_u32_e32 v3, 0x1400, v74
	ds_write2_b32 v2, v6, v7 offset1:32
	ds_write2_b32 v3, v22, v23 offset1:32
	ds_write2_b32 v2, v8, v9 offset0:64 offset1:96
	ds_write2_b32 v3, v24, v25 offset0:64 offset1:96
	v_add_u32_e32 v2, 0x800, v74
	v_add_u32_e32 v3, 0x1800, v74
	ds_write2_b32 v2, v10, v11 offset1:32
	ds_write2_b32 v3, v26, v27 offset1:32
	ds_write2_b32 v2, v12, v13 offset0:64 offset1:96
	ds_write2_b32 v3, v28, v29 offset0:64 offset1:96
	v_add_u32_e32 v2, 0xc00, v74
	v_add_u32_e32 v3, 0x1c00, v74
	ds_write2_b32 v2, v14, v15 offset1:32
	ds_write2_b32 v3, v30, v31 offset1:32
	ds_write2_b32 v2, v16, v17 offset0:64 offset1:96
	ds_write2_b32 v3, v32, v33 offset0:64 offset1:96
	s_waitcnt lgkmcnt(0)
	s_barrier
	ds_read2st64_b32 v[2:3], v76 offset1:32
	ds_read2st64_b32 v[4:5], v76 offset0:64 offset1:96
	ds_read2st64_b32 v[6:7], v76 offset0:128 offset1:160
	s_waitcnt lgkmcnt(2)
	v_add_f32_e32 v2, 0, v2
	v_add_f32_e32 v8, v2, v3
	ds_read2st64_b32 v[2:3], v76 offset0:192 offset1:224
	s_waitcnt lgkmcnt(2)
	v_add_f32_e32 v4, v8, v4
	v_add_f32_e32 v4, v4, v5
	s_waitcnt lgkmcnt(1)
	v_add_f32_e32 v4, v4, v6
	v_add_f32_e32 v4, v4, v7
	s_waitcnt lgkmcnt(0)
	v_add_f32_e32 v2, v4, v2
	v_add_f32_e32 v14, v2, v3
	ds_read_b64 v[2:3], v138
	ds_read2_b32 v[4:5], v75 offset1:32
	ds_read2st64_b32 v[6:7], v78 offset1:32
	ds_read_b64 v[8:9], v139
	ds_read_b64 v[10:11], v140
	ds_read_b64 v[12:13], v141
	s_waitcnt lgkmcnt(4)
	v_fma_f32 v2, -v2, v4, v14
	v_fma_f32 v2, v3, v2, v5
	ds_write_b32 v77, v2
	ds_read2st64_b32 v[2:3], v78 offset0:64 offset1:96
	ds_read2st64_b32 v[14:15], v78 offset0:128 offset1:160
	s_waitcnt lgkmcnt(6)
	v_add_f32_e32 v6, 0, v6
	v_add_f32_e32 v16, v6, v7
	ds_read2st64_b32 v[6:7], v78 offset0:192 offset1:224
	s_waitcnt lgkmcnt(2)
	v_add_f32_e32 v2, v16, v2
	v_add_f32_e32 v2, v2, v3
	s_waitcnt lgkmcnt(1)
	v_add_f32_e32 v2, v2, v14
	v_add_f32_e32 v2, v2, v15
	s_waitcnt lgkmcnt(0)
	v_add_f32_e32 v2, v2, v6
	v_add_f32_e32 v6, v2, v7
	ds_read2st64_b32 v[2:3], v80 offset1:32
	v_fma_f32 v6, -v4, v8, v6
	v_fma_f32 v6, v9, v6, v5
	ds_write_b32 v79, v6
	ds_read2st64_b32 v[6:7], v80 offset0:64 offset1:96
	ds_read2st64_b32 v[8:9], v80 offset0:128 offset1:160
	s_waitcnt lgkmcnt(3)
	v_add_f32_e32 v2, 0, v2
	v_add_f32_e32 v14, v2, v3
	ds_read2st64_b32 v[2:3], v80 offset0:192 offset1:224
	s_waitcnt lgkmcnt(2)
	v_add_f32_e32 v6, v14, v6
	v_add_f32_e32 v6, v6, v7
	s_waitcnt lgkmcnt(1)
	v_add_f32_e32 v6, v6, v8
	v_add_f32_e32 v6, v6, v9
	s_waitcnt lgkmcnt(0)
	v_add_f32_e32 v2, v6, v2
	v_add_f32_e32 v6, v2, v3
	ds_read2st64_b32 v[2:3], v82 offset1:32
	v_fma_f32 v6, -v4, v10, v6
	v_fma_f32 v6, v11, v6, v5
	ds_write_b32 v81, v6
	ds_read2st64_b32 v[6:7], v82 offset0:64 offset1:96
	ds_read2st64_b32 v[8:9], v82 offset0:128 offset1:160
	s_waitcnt lgkmcnt(3)
	v_add_f32_e32 v2, 0, v2
	v_add_f32_e32 v10, v2, v3
	ds_read2st64_b32 v[2:3], v82 offset0:192 offset1:224
	s_waitcnt lgkmcnt(2)
	v_add_f32_e32 v6, v10, v6
	v_add_f32_e32 v6, v6, v7
	s_waitcnt lgkmcnt(1)
	v_add_f32_e32 v6, v6, v8
	v_add_f32_e32 v6, v6, v9
	s_waitcnt lgkmcnt(0)
	v_add_f32_e32 v2, v6, v2
	v_add_f32_e32 v2, v2, v3
	v_fma_f32 v2, -v4, v12, v2
	v_fmac_f32_e32 v5, v13, v2
	ds_write_b32 v83, v5
	s_waitcnt lgkmcnt(0)
	s_barrier
	s_and_saveexec_b64 s[36:37], s[82:83]
	s_cbranch_execz .LBB0_714
	ds_read_b32 v52, v84
	ds_read_b32 v34, v85
	ds_read_b32 v33, v86
	ds_read_b32 v32, v87
	ds_read_b32 v31, v88
	ds_read_b32 v30, v89
	ds_read_b32 v29, v90
	ds_read_b32 v28, v91
	ds_read_b32 v27, v92
	ds_read_b32 v26, v93
	ds_read_b32 v25, v94
	ds_read_b32 v24, v95
	ds_read_b32 v23, v96
	ds_read_b32 v22, v97
	ds_read_b32 v21, v98
	ds_read_b32 v20, v99
	ds_read_b32 v18, v100
	ds_read_b32 v17, v101
	ds_read_b32 v16, v102
	ds_read_b32 v15, v103
	ds_read_b32 v14, v104
	ds_read_b32 v13, v105
	ds_read_b32 v11, v106
	ds_read_b32 v10, v107
	ds_read_b32 v9, v108
	ds_read_b32 v8, v109
	ds_read_b32 v7, v110
	ds_read_b32 v6, v111
	ds_read_b32 v5, v112
	ds_read_b32 v4, v113
	ds_read_b32 v3, v114
	ds_read_b32 v2, v115
	s_waitcnt lgkmcnt(14)
	v_cmp_lg_f32_e32 vcc, s48, v52
	s_nop 1
	v_cndmask_b32_e32 v12, v143, v52, vcc
	v_cmp_gt_f32_e32 vcc, v34, v12
	s_nop 1
	v_cndmask_b32_e32 v12, v12, v34, vcc
	v_cndmask_b32_e64 v19, 0, 1, vcc
	v_cmp_gt_f32_e32 vcc, v33, v12
	s_nop 1
	v_cndmask_b32_e32 v12, v12, v33, vcc
	v_cndmask_b32_e64 v19, v19, 2, vcc
	v_cmp_gt_f32_e32 vcc, v32, v12
	s_nop 1
	v_cndmask_b32_e32 v12, v12, v32, vcc
	v_cndmask_b32_e64 v19, v19, 3, vcc
	v_cmp_gt_f32_e32 vcc, v31, v12
	s_nop 1
	v_cndmask_b32_e32 v12, v12, v31, vcc
	v_cndmask_b32_e64 v19, v19, 4, vcc
	v_cmp_gt_f32_e32 vcc, v30, v12
	s_nop 1
	v_cndmask_b32_e32 v12, v12, v30, vcc
	v_cndmask_b32_e64 v19, v19, 5, vcc
	v_cmp_gt_f32_e32 vcc, v29, v12
	s_nop 1
	v_cndmask_b32_e32 v12, v12, v29, vcc
	v_cndmask_b32_e64 v19, v19, 6, vcc
	v_cmp_gt_f32_e32 vcc, v28, v12
	s_nop 1
	v_cndmask_b32_e32 v12, v12, v28, vcc
	v_cndmask_b32_e64 v19, v19, 7, vcc
	v_cmp_gt_f32_e32 vcc, v27, v12
	s_nop 1
	v_cndmask_b32_e32 v12, v12, v27, vcc
	v_cndmask_b32_e64 v19, v19, 8, vcc
	v_cmp_gt_f32_e32 vcc, v26, v12
	s_nop 1
	v_cndmask_b32_e32 v12, v12, v26, vcc
	v_cndmask_b32_e64 v19, v19, 9, vcc
	v_cmp_gt_f32_e32 vcc, v25, v12
	s_nop 1
	v_cndmask_b32_e32 v12, v12, v25, vcc
	v_cndmask_b32_e64 v19, v19, 10, vcc
	v_cmp_gt_f32_e32 vcc, v24, v12
	s_nop 1
	v_cndmask_b32_e32 v12, v12, v24, vcc
	v_cndmask_b32_e64 v19, v19, 11, vcc
	v_cmp_gt_f32_e32 vcc, v23, v12
	s_nop 1
	v_cndmask_b32_e32 v12, v12, v23, vcc
	v_cndmask_b32_e64 v19, v19, 12, vcc
	v_cmp_gt_f32_e32 vcc, v22, v12
	s_nop 1
	v_cndmask_b32_e32 v12, v12, v22, vcc
	v_cndmask_b32_e64 v19, v19, 13, vcc
	v_cmp_gt_f32_e32 vcc, v21, v12
	s_nop 1
	v_cndmask_b32_e32 v12, v12, v21, vcc
	v_cndmask_b32_e64 v19, v19, 14, vcc
	v_cmp_gt_f32_e32 vcc, v20, v12
	s_nop 1
	v_cndmask_b32_e32 v12, v12, v20, vcc
	v_cndmask_b32_e64 v19, v19, 15, vcc
	v_cmp_gt_f32_e32 vcc, v18, v12
	s_nop 1
	v_cndmask_b32_e32 v12, v12, v18, vcc
	v_cndmask_b32_e64 v19, v19, 16, vcc
	v_cmp_gt_f32_e32 vcc, v17, v12
	s_nop 1
	v_cndmask_b32_e32 v12, v12, v17, vcc
	v_cndmask_b32_e64 v19, v19, 17, vcc
	s_waitcnt lgkmcnt(13)
	v_cmp_gt_f32_e32 vcc, v16, v12
	s_nop 1
	v_cndmask_b32_e32 v12, v12, v16, vcc
	v_cndmask_b32_e64 v19, v19, 18, vcc
	s_waitcnt lgkmcnt(12)
	v_cmp_gt_f32_e32 vcc, v15, v12
	s_nop 1
	v_cndmask_b32_e32 v12, v12, v15, vcc
	v_cndmask_b32_e64 v19, v19, 19, vcc
	s_waitcnt lgkmcnt(11)
	v_cmp_gt_f32_e32 vcc, v14, v12
	s_nop 1
	v_cndmask_b32_e32 v12, v12, v14, vcc
	v_cndmask_b32_e64 v19, v19, 20, vcc
	s_waitcnt lgkmcnt(10)
	v_cmp_gt_f32_e32 vcc, v13, v12
	s_nop 1
	v_cndmask_b32_e32 v12, v12, v13, vcc
	v_cndmask_b32_e64 v19, v19, 21, vcc
	s_waitcnt lgkmcnt(9)
	v_cmp_gt_f32_e32 vcc, v11, v12
	s_nop 1
	v_cndmask_b32_e32 v12, v12, v11, vcc
	v_cndmask_b32_e64 v19, v19, 22, vcc
	s_waitcnt lgkmcnt(8)
	v_cmp_gt_f32_e32 vcc, v10, v12
	s_nop 1
	v_cndmask_b32_e32 v12, v12, v10, vcc
	v_cndmask_b32_e64 v19, v19, 23, vcc
	s_waitcnt lgkmcnt(7)
	v_cmp_gt_f32_e32 vcc, v9, v12
	s_nop 1
	v_cndmask_b32_e32 v12, v12, v9, vcc
	v_cndmask_b32_e64 v19, v19, 24, vcc
	s_waitcnt lgkmcnt(6)
	v_cmp_gt_f32_e32 vcc, v8, v12
	s_nop 1
	v_cndmask_b32_e32 v12, v12, v8, vcc
	v_cndmask_b32_e64 v19, v19, 25, vcc
	s_waitcnt lgkmcnt(5)
	v_cmp_gt_f32_e32 vcc, v7, v12
	s_nop 1
	v_cndmask_b32_e32 v12, v12, v7, vcc
	v_cndmask_b32_e64 v19, v19, 26, vcc
	s_waitcnt lgkmcnt(4)
	v_cmp_gt_f32_e32 vcc, v6, v12
	s_nop 1
	v_cndmask_b32_e32 v12, v12, v6, vcc
	v_cndmask_b32_e64 v19, v19, 27, vcc
	s_waitcnt lgkmcnt(3)
	v_cmp_gt_f32_e32 vcc, v5, v12
	s_nop 1
	v_cndmask_b32_e32 v12, v12, v5, vcc
	v_cndmask_b32_e64 v19, v19, 28, vcc
	s_waitcnt lgkmcnt(2)
	v_cmp_gt_f32_e32 vcc, v4, v12
	s_nop 1
	v_cndmask_b32_e32 v12, v12, v4, vcc
	v_cndmask_b32_e64 v19, v19, 29, vcc
	s_waitcnt lgkmcnt(1)
	v_cmp_gt_f32_e32 vcc, v3, v12
	s_nop 1
	v_cndmask_b32_e32 v53, v12, v3, vcc
	v_cndmask_b32_e64 v19, v19, 30, vcc
	s_waitcnt lgkmcnt(0)
	v_cmp_gt_f32_e32 vcc, v2, v53
	s_nop 1
	v_cndmask_b32_e64 v12, v19, 31, vcc
	v_cndmask_b32_e32 v19, v53, v2, vcc
	v_cmp_eq_u32_e64 s[12:13], 0, v12
	v_cmp_nlg_f32_e32 vcc, s48, v52
	v_lshlrev_b32_e64 v53, v12, 1
	s_or_b64 s[12:13], s[12:13], vcc
	v_cndmask_b32_e64 v54, v52, v143, s[12:13]
	v_and_b32_e32 v55, 2, v53
	v_cmp_eq_u32_e64 s[12:13], 0, v55
	v_cmp_gt_f32_e64 s[14:15], v34, v54
	s_and_b64 s[12:13], s[12:13], s[14:15]
	v_cndmask_b32_e64 v54, v54, v34, s[12:13]
	v_and_b32_e32 v56, 4, v53
	v_cndmask_b32_e64 v55, 0, 1, s[12:13]
	v_cmp_eq_u32_e64 s[12:13], 0, v56
	v_cmp_gt_f32_e64 s[14:15], v33, v54
	s_and_b64 s[12:13], s[12:13], s[14:15]
	v_cndmask_b32_e64 v54, v54, v33, s[12:13]
	v_and_b32_e32 v56, 8, v53
	v_cndmask_b32_e64 v55, v55, 2, s[12:13]
	v_cmp_eq_u32_e64 s[12:13], 0, v56
	v_cmp_gt_f32_e64 s[14:15], v32, v54
	s_and_b64 s[12:13], s[12:13], s[14:15]
	v_cndmask_b32_e64 v54, v54, v32, s[12:13]
	v_and_b32_e32 v56, 16, v53
	v_cndmask_b32_e64 v55, v55, 3, s[12:13]
	v_cmp_eq_u32_e64 s[12:13], 0, v56
	v_cmp_gt_f32_e64 s[14:15], v31, v54
	s_and_b64 s[12:13], s[12:13], s[14:15]
	v_cndmask_b32_e64 v54, v54, v31, s[12:13]
	v_and_b32_e32 v56, 32, v53
	v_cndmask_b32_e64 v55, v55, 4, s[12:13]
	v_cmp_eq_u32_e64 s[12:13], 0, v56
	v_cmp_gt_f32_e64 s[14:15], v30, v54
	s_and_b64 s[12:13], s[12:13], s[14:15]
	v_cndmask_b32_e64 v54, v54, v30, s[12:13]
	v_and_b32_e32 v56, 64, v53
	v_cndmask_b32_e64 v55, v55, 5, s[12:13]
	v_cmp_eq_u32_e64 s[12:13], 0, v56
	v_cmp_gt_f32_e64 s[14:15], v29, v54
	s_and_b64 s[12:13], s[12:13], s[14:15]
	v_cndmask_b32_e64 v54, v54, v29, s[12:13]
	v_and_b32_e32 v56, 0x80, v53
	v_cndmask_b32_e64 v55, v55, 6, s[12:13]
	v_cmp_eq_u32_e64 s[12:13], 0, v56
	v_cmp_gt_f32_e64 s[14:15], v28, v54
	s_and_b64 s[12:13], s[12:13], s[14:15]
	v_cndmask_b32_e64 v54, v54, v28, s[12:13]
	v_and_b32_e32 v56, 0x100, v53
	v_cndmask_b32_e64 v55, v55, 7, s[12:13]
	v_cmp_eq_u32_e64 s[12:13], 0, v56
	v_cmp_gt_f32_e64 s[14:15], v27, v54
	s_and_b64 s[12:13], s[12:13], s[14:15]
	v_cndmask_b32_e64 v54, v54, v27, s[12:13]
	v_and_b32_e32 v56, 0x200, v53
	v_cndmask_b32_e64 v55, v55, 8, s[12:13]
	v_cmp_eq_u32_e64 s[12:13], 0, v56
	v_cmp_gt_f32_e64 s[14:15], v26, v54
	s_and_b64 s[12:13], s[12:13], s[14:15]
	v_cndmask_b32_e64 v54, v54, v26, s[12:13]
	v_and_b32_e32 v56, 0x400, v53
	v_cndmask_b32_e64 v55, v55, 9, s[12:13]
	v_cmp_eq_u32_e64 s[12:13], 0, v56
	v_cmp_gt_f32_e64 s[14:15], v25, v54
	s_and_b64 s[12:13], s[12:13], s[14:15]
	v_cndmask_b32_e64 v54, v54, v25, s[12:13]
	v_and_b32_e32 v56, 0x800, v53
	v_cndmask_b32_e64 v55, v55, 10, s[12:13]
	v_cmp_eq_u32_e64 s[12:13], 0, v56
	v_cmp_gt_f32_e64 s[14:15], v24, v54
	s_and_b64 s[12:13], s[12:13], s[14:15]
	v_cndmask_b32_e64 v54, v54, v24, s[12:13]
	v_and_b32_e32 v56, 0x1000, v53
	v_cndmask_b32_e64 v55, v55, 11, s[12:13]
	v_cmp_eq_u32_e64 s[12:13], 0, v56
	v_cmp_gt_f32_e64 s[14:15], v23, v54
	s_and_b64 s[12:13], s[12:13], s[14:15]
	v_cndmask_b32_e64 v54, v54, v23, s[12:13]
	v_and_b32_e32 v56, 0x2000, v53
	v_cndmask_b32_e64 v55, v55, 12, s[12:13]
	v_cmp_eq_u32_e64 s[12:13], 0, v56
	v_cmp_gt_f32_e64 s[14:15], v22, v54
	s_and_b64 s[12:13], s[12:13], s[14:15]
	v_cndmask_b32_e64 v54, v54, v22, s[12:13]
	v_and_b32_e32 v56, 0x4000, v53
	v_cndmask_b32_e64 v55, v55, 13, s[12:13]
	v_cmp_eq_u32_e64 s[12:13], 0, v56
	v_cmp_gt_f32_e64 s[14:15], v21, v54
	s_and_b64 s[12:13], s[12:13], s[14:15]
	v_cndmask_b32_e64 v54, v54, v21, s[12:13]
	v_and_b32_e32 v56, 0x8000, v53
	v_cndmask_b32_e64 v55, v55, 14, s[12:13]
	v_cmp_eq_u32_e64 s[12:13], 0, v56
	v_cmp_gt_f32_e64 s[14:15], v20, v54
	s_and_b64 s[12:13], s[12:13], s[14:15]
	v_cndmask_b32_e64 v54, v54, v20, s[12:13]
	v_and_b32_e32 v56, 0x10000, v53
	v_cndmask_b32_e64 v55, v55, 15, s[12:13]
	v_cmp_eq_u32_e64 s[12:13], 0, v56
	v_cmp_gt_f32_e64 s[14:15], v18, v54
	s_and_b64 s[12:13], s[12:13], s[14:15]
	v_cndmask_b32_e64 v54, v54, v18, s[12:13]
	v_and_b32_e32 v56, 0x20000, v53
	v_cndmask_b32_e64 v55, v55, 16, s[12:13]
	v_cmp_eq_u32_e64 s[12:13], 0, v56
	v_cmp_gt_f32_e64 s[14:15], v17, v54
	s_and_b64 s[12:13], s[12:13], s[14:15]
	v_cndmask_b32_e64 v54, v54, v17, s[12:13]
	v_and_b32_e32 v56, 0x40000, v53
	v_cndmask_b32_e64 v55, v55, 17, s[12:13]
	v_cmp_eq_u32_e64 s[12:13], 0, v56
	v_cmp_gt_f32_e64 s[14:15], v16, v54
	s_and_b64 s[12:13], s[12:13], s[14:15]
	v_cndmask_b32_e64 v54, v54, v16, s[12:13]
	v_and_b32_e32 v56, 0x80000, v53
	v_cndmask_b32_e64 v55, v55, 18, s[12:13]
	v_cmp_eq_u32_e64 s[12:13], 0, v56
	v_cmp_gt_f32_e64 s[14:15], v15, v54
	s_and_b64 s[12:13], s[12:13], s[14:15]
	v_cndmask_b32_e64 v54, v54, v15, s[12:13]
	v_and_b32_e32 v56, 0x100000, v53
	v_cndmask_b32_e64 v55, v55, 19, s[12:13]
	v_cmp_eq_u32_e64 s[12:13], 0, v56
	v_cmp_gt_f32_e64 s[14:15], v14, v54
	s_and_b64 s[12:13], s[12:13], s[14:15]
	v_cndmask_b32_e64 v54, v54, v14, s[12:13]
	v_and_b32_e32 v56, 0x200000, v53
	v_cndmask_b32_e64 v55, v55, 20, s[12:13]
	v_cmp_eq_u32_e64 s[12:13], 0, v56
	v_cmp_gt_f32_e64 s[14:15], v13, v54
	s_and_b64 s[12:13], s[12:13], s[14:15]
	v_cndmask_b32_e64 v54, v54, v13, s[12:13]
	v_and_b32_e32 v56, 0x400000, v53
	v_cndmask_b32_e64 v55, v55, 21, s[12:13]
	v_cmp_eq_u32_e64 s[12:13], 0, v56
	v_cmp_gt_f32_e64 s[14:15], v11, v54
	s_and_b64 s[12:13], s[12:13], s[14:15]
	v_cndmask_b32_e64 v54, v54, v11, s[12:13]
	v_and_b32_e32 v56, 0x800000, v53
	v_cndmask_b32_e64 v55, v55, 22, s[12:13]
	v_cmp_eq_u32_e64 s[12:13], 0, v56
	v_cmp_gt_f32_e64 s[14:15], v10, v54
	s_and_b64 s[12:13], s[12:13], s[14:15]
	v_cndmask_b32_e64 v54, v54, v10, s[12:13]
	v_and_b32_e32 v56, 0x1000000, v53
	v_cndmask_b32_e64 v55, v55, 23, s[12:13]
	v_cmp_eq_u32_e64 s[12:13], 0, v56
	v_cmp_gt_f32_e64 s[14:15], v9, v54
	s_and_b64 s[12:13], s[12:13], s[14:15]
	v_cndmask_b32_e64 v54, v54, v9, s[12:13]
	v_and_b32_e32 v56, 0x2000000, v53
	v_cndmask_b32_e64 v55, v55, 24, s[12:13]
	v_cmp_eq_u32_e64 s[12:13], 0, v56
	v_cmp_gt_f32_e64 s[14:15], v8, v54
	s_and_b64 s[12:13], s[12:13], s[14:15]
	v_cndmask_b32_e64 v54, v54, v8, s[12:13]
	v_and_b32_e32 v56, 0x4000000, v53
	v_cndmask_b32_e64 v55, v55, 25, s[12:13]
	v_cmp_eq_u32_e64 s[12:13], 0, v56
	v_cmp_gt_f32_e64 s[14:15], v7, v54
	s_and_b64 s[12:13], s[12:13], s[14:15]
	v_cndmask_b32_e64 v54, v54, v7, s[12:13]
	v_and_b32_e32 v56, 0x8000000, v53
	v_cndmask_b32_e64 v55, v55, 26, s[12:13]
	v_cmp_eq_u32_e64 s[12:13], 0, v56
	v_cmp_gt_f32_e64 s[14:15], v6, v54
	s_and_b64 s[12:13], s[12:13], s[14:15]
	v_cndmask_b32_e64 v54, v54, v6, s[12:13]
	v_and_b32_e32 v56, 0x10000000, v53
	v_cndmask_b32_e64 v55, v55, 27, s[12:13]
	v_cmp_eq_u32_e64 s[12:13], 0, v56
	v_cmp_gt_f32_e64 s[14:15], v5, v54
	s_and_b64 s[12:13], s[12:13], s[14:15]
	v_cndmask_b32_e64 v54, v54, v5, s[12:13]
	v_and_b32_e32 v56, 0x20000000, v53
	v_cndmask_b32_e64 v55, v55, 28, s[12:13]
	v_cmp_eq_u32_e64 s[12:13], 0, v56
	v_cmp_gt_f32_e64 s[14:15], v4, v54
	s_and_b64 s[12:13], s[12:13], s[14:15]
	v_cndmask_b32_e64 v54, v54, v4, s[12:13]
	v_and_b32_e32 v56, 2.0, v53
	v_cndmask_b32_e64 v55, v55, 29, s[12:13]
	v_cmp_eq_u32_e64 s[12:13], 0, v56
	v_cmp_gt_f32_e64 s[14:15], v3, v54
	s_and_b64 s[12:13], s[12:13], s[14:15]
	v_cndmask_b32_e64 v54, v54, v3, s[12:13]
	v_cndmask_b32_e64 v55, v55, 30, s[12:13]
	v_cmp_ne_u32_e64 s[12:13], 31, v12
	v_cmp_gt_f32_e64 s[14:15], v2, v54
	s_and_b64 s[12:13], s[12:13], s[14:15]
	v_cndmask_b32_e64 v55, v55, 31, s[12:13]
	v_lshl_or_b32 v53, 1, v55, v53
	v_and_b32_e32 v56, 1, v53
	v_cndmask_b32_e64 v54, v54, v2, s[12:13]
	v_cmp_eq_u32_e64 s[12:13], 1, v56
	s_or_b64 s[12:13], s[12:13], vcc
	v_and_b32_e32 v57, 2, v53
	v_cndmask_b32_e64 v56, v52, v143, s[12:13]
	v_cmp_eq_u32_e64 s[12:13], 0, v57
	v_cmp_gt_f32_e64 s[14:15], v34, v56
	s_and_b64 s[12:13], s[12:13], s[14:15]
	v_cndmask_b32_e64 v56, v56, v34, s[12:13]
	v_and_b32_e32 v58, 4, v53
	v_cndmask_b32_e64 v57, 0, 1, s[12:13]
	v_cmp_eq_u32_e64 s[12:13], 0, v58
	v_cmp_gt_f32_e64 s[14:15], v33, v56
	s_and_b64 s[12:13], s[12:13], s[14:15]
	v_cndmask_b32_e64 v56, v56, v33, s[12:13]
	v_and_b32_e32 v58, 8, v53
	v_cndmask_b32_e64 v57, v57, 2, s[12:13]
	v_cmp_eq_u32_e64 s[12:13], 0, v58
	v_cmp_gt_f32_e64 s[14:15], v32, v56
	s_and_b64 s[12:13], s[12:13], s[14:15]
	v_cndmask_b32_e64 v56, v56, v32, s[12:13]
	v_and_b32_e32 v58, 16, v53
	v_cndmask_b32_e64 v57, v57, 3, s[12:13]
	v_cmp_eq_u32_e64 s[12:13], 0, v58
	v_cmp_gt_f32_e64 s[14:15], v31, v56
	s_and_b64 s[12:13], s[12:13], s[14:15]
	v_cndmask_b32_e64 v56, v56, v31, s[12:13]
	v_and_b32_e32 v58, 32, v53
	v_cndmask_b32_e64 v57, v57, 4, s[12:13]
	v_cmp_eq_u32_e64 s[12:13], 0, v58
	v_cmp_gt_f32_e64 s[14:15], v30, v56
	s_and_b64 s[12:13], s[12:13], s[14:15]
	v_cndmask_b32_e64 v56, v56, v30, s[12:13]
	v_and_b32_e32 v58, 64, v53
	v_cndmask_b32_e64 v57, v57, 5, s[12:13]
	v_cmp_eq_u32_e64 s[12:13], 0, v58
	v_cmp_gt_f32_e64 s[14:15], v29, v56
	s_and_b64 s[12:13], s[12:13], s[14:15]
	v_cndmask_b32_e64 v56, v56, v29, s[12:13]
	v_and_b32_e32 v58, 0x80, v53
	v_cndmask_b32_e64 v57, v57, 6, s[12:13]
	v_cmp_eq_u32_e64 s[12:13], 0, v58
	v_cmp_gt_f32_e64 s[14:15], v28, v56
	s_and_b64 s[12:13], s[12:13], s[14:15]
	v_cndmask_b32_e64 v56, v56, v28, s[12:13]
	v_and_b32_e32 v58, 0x100, v53
	v_cndmask_b32_e64 v57, v57, 7, s[12:13]
	v_cmp_eq_u32_e64 s[12:13], 0, v58
	v_cmp_gt_f32_e64 s[14:15], v27, v56
	s_and_b64 s[12:13], s[12:13], s[14:15]
	v_cndmask_b32_e64 v56, v56, v27, s[12:13]
	v_and_b32_e32 v58, 0x200, v53
	v_cndmask_b32_e64 v57, v57, 8, s[12:13]
	v_cmp_eq_u32_e64 s[12:13], 0, v58
	v_cmp_gt_f32_e64 s[14:15], v26, v56
	s_and_b64 s[12:13], s[12:13], s[14:15]
	v_cndmask_b32_e64 v56, v56, v26, s[12:13]
	v_and_b32_e32 v58, 0x400, v53
	v_cndmask_b32_e64 v57, v57, 9, s[12:13]
	v_cmp_eq_u32_e64 s[12:13], 0, v58
	v_cmp_gt_f32_e64 s[14:15], v25, v56
	s_and_b64 s[12:13], s[12:13], s[14:15]
	v_cndmask_b32_e64 v56, v56, v25, s[12:13]
	v_and_b32_e32 v58, 0x800, v53
	v_cndmask_b32_e64 v57, v57, 10, s[12:13]
	v_cmp_eq_u32_e64 s[12:13], 0, v58
	v_cmp_gt_f32_e64 s[14:15], v24, v56
	s_and_b64 s[12:13], s[12:13], s[14:15]
	v_cndmask_b32_e64 v56, v56, v24, s[12:13]
	v_and_b32_e32 v58, 0x1000, v53
	v_cndmask_b32_e64 v57, v57, 11, s[12:13]
	v_cmp_eq_u32_e64 s[12:13], 0, v58
	v_cmp_gt_f32_e64 s[14:15], v23, v56
	s_and_b64 s[12:13], s[12:13], s[14:15]
	v_cndmask_b32_e64 v56, v56, v23, s[12:13]
	v_and_b32_e32 v58, 0x2000, v53
	v_cndmask_b32_e64 v57, v57, 12, s[12:13]
	v_cmp_eq_u32_e64 s[12:13], 0, v58
	v_cmp_gt_f32_e64 s[14:15], v22, v56
	s_and_b64 s[12:13], s[12:13], s[14:15]
	v_cndmask_b32_e64 v56, v56, v22, s[12:13]
	v_and_b32_e32 v58, 0x4000, v53
	v_cndmask_b32_e64 v57, v57, 13, s[12:13]
	v_cmp_eq_u32_e64 s[12:13], 0, v58
	v_cmp_gt_f32_e64 s[14:15], v21, v56
	s_and_b64 s[12:13], s[12:13], s[14:15]
	v_cndmask_b32_e64 v56, v56, v21, s[12:13]
	v_and_b32_e32 v58, 0x8000, v53
	v_cndmask_b32_e64 v57, v57, 14, s[12:13]
	v_cmp_eq_u32_e64 s[12:13], 0, v58
	v_cmp_gt_f32_e64 s[14:15], v20, v56
	s_and_b64 s[12:13], s[12:13], s[14:15]
	v_cndmask_b32_e64 v56, v56, v20, s[12:13]
	v_and_b32_e32 v58, 0x10000, v53
	v_cndmask_b32_e64 v57, v57, 15, s[12:13]
	v_cmp_eq_u32_e64 s[12:13], 0, v58
	v_cmp_gt_f32_e64 s[14:15], v18, v56
	s_and_b64 s[12:13], s[12:13], s[14:15]
	v_cndmask_b32_e64 v56, v56, v18, s[12:13]
	v_and_b32_e32 v58, 0x20000, v53
	v_cndmask_b32_e64 v57, v57, 16, s[12:13]
	v_cmp_eq_u32_e64 s[12:13], 0, v58
	v_cmp_gt_f32_e64 s[14:15], v17, v56
	s_and_b64 s[12:13], s[12:13], s[14:15]
	v_cndmask_b32_e64 v56, v56, v17, s[12:13]
	v_and_b32_e32 v58, 0x40000, v53
	v_cndmask_b32_e64 v57, v57, 17, s[12:13]
	v_cmp_eq_u32_e64 s[12:13], 0, v58
	v_cmp_gt_f32_e64 s[14:15], v16, v56
	s_and_b64 s[12:13], s[12:13], s[14:15]
	v_cndmask_b32_e64 v56, v56, v16, s[12:13]
	v_and_b32_e32 v58, 0x80000, v53
	v_cndmask_b32_e64 v57, v57, 18, s[12:13]
	v_cmp_eq_u32_e64 s[12:13], 0, v58
	v_cmp_gt_f32_e64 s[14:15], v15, v56
	s_and_b64 s[12:13], s[12:13], s[14:15]
	v_cndmask_b32_e64 v56, v56, v15, s[12:13]
	v_and_b32_e32 v58, 0x100000, v53
	v_cndmask_b32_e64 v57, v57, 19, s[12:13]
	v_cmp_eq_u32_e64 s[12:13], 0, v58
	v_cmp_gt_f32_e64 s[14:15], v14, v56
	s_and_b64 s[12:13], s[12:13], s[14:15]
	v_cndmask_b32_e64 v56, v56, v14, s[12:13]
	v_and_b32_e32 v58, 0x200000, v53
	v_cndmask_b32_e64 v57, v57, 20, s[12:13]
	v_cmp_eq_u32_e64 s[12:13], 0, v58
	v_cmp_gt_f32_e64 s[14:15], v13, v56
	s_and_b64 s[12:13], s[12:13], s[14:15]
	v_cndmask_b32_e64 v56, v56, v13, s[12:13]
	v_and_b32_e32 v58, 0x400000, v53
	v_cndmask_b32_e64 v57, v57, 21, s[12:13]
	v_cmp_eq_u32_e64 s[12:13], 0, v58
	v_cmp_gt_f32_e64 s[14:15], v11, v56
	s_and_b64 s[12:13], s[12:13], s[14:15]
	v_cndmask_b32_e64 v56, v56, v11, s[12:13]
	v_and_b32_e32 v58, 0x800000, v53
	v_cndmask_b32_e64 v57, v57, 22, s[12:13]
	v_cmp_eq_u32_e64 s[12:13], 0, v58
	v_cmp_gt_f32_e64 s[14:15], v10, v56
	s_and_b64 s[12:13], s[12:13], s[14:15]
	v_cndmask_b32_e64 v56, v56, v10, s[12:13]
	v_and_b32_e32 v58, 0x1000000, v53
	v_cndmask_b32_e64 v57, v57, 23, s[12:13]
	v_cmp_eq_u32_e64 s[12:13], 0, v58
	v_cmp_gt_f32_e64 s[14:15], v9, v56
	s_and_b64 s[12:13], s[12:13], s[14:15]
	v_cndmask_b32_e64 v56, v56, v9, s[12:13]
	v_and_b32_e32 v58, 0x2000000, v53
	v_cndmask_b32_e64 v57, v57, 24, s[12:13]
	v_cmp_eq_u32_e64 s[12:13], 0, v58
	v_cmp_gt_f32_e64 s[14:15], v8, v56
	s_and_b64 s[12:13], s[12:13], s[14:15]
	v_cndmask_b32_e64 v56, v56, v8, s[12:13]
	v_and_b32_e32 v58, 0x4000000, v53
	v_cndmask_b32_e64 v57, v57, 25, s[12:13]
	v_cmp_eq_u32_e64 s[12:13], 0, v58
	v_cmp_gt_f32_e64 s[14:15], v7, v56
	s_and_b64 s[12:13], s[12:13], s[14:15]
	v_cndmask_b32_e64 v56, v56, v7, s[12:13]
	v_and_b32_e32 v58, 0x8000000, v53
	v_cndmask_b32_e64 v57, v57, 26, s[12:13]
	v_cmp_eq_u32_e64 s[12:13], 0, v58
	v_cmp_gt_f32_e64 s[14:15], v6, v56
	s_and_b64 s[12:13], s[12:13], s[14:15]
	v_cndmask_b32_e64 v56, v56, v6, s[12:13]
	v_and_b32_e32 v58, 0x10000000, v53
	v_cndmask_b32_e64 v57, v57, 27, s[12:13]
	v_cmp_eq_u32_e64 s[12:13], 0, v58
	v_cmp_gt_f32_e64 s[14:15], v5, v56
	s_and_b64 s[12:13], s[12:13], s[14:15]
	v_cndmask_b32_e64 v56, v56, v5, s[12:13]
	v_and_b32_e32 v58, 0x20000000, v53
	v_cndmask_b32_e64 v57, v57, 28, s[12:13]
	v_cmp_eq_u32_e64 s[12:13], 0, v58
	v_cmp_gt_f32_e64 s[14:15], v4, v56
	s_and_b64 s[12:13], s[12:13], s[14:15]
	v_cndmask_b32_e64 v56, v56, v4, s[12:13]
	v_and_b32_e32 v58, 2.0, v53
	v_cndmask_b32_e64 v57, v57, 29, s[12:13]
	v_cmp_eq_u32_e64 s[12:13], 0, v58
	v_cmp_gt_f32_e64 s[14:15], v3, v56
	s_and_b64 s[12:13], s[12:13], s[14:15]
	v_cndmask_b32_e64 v56, v56, v3, s[12:13]
	v_cndmask_b32_e64 v57, v57, 30, s[12:13]
	v_cmp_lt_i32_e64 s[12:13], -1, v53
	v_cmp_gt_f32_e64 s[14:15], v2, v56
	s_and_b64 s[12:13], s[12:13], s[14:15]
	v_cndmask_b32_e64 v57, v57, 31, s[12:13]
	v_lshlrev_b32_e64 v58, v57, 1
	v_or_b32_e32 v59, v58, v53
	v_and_b32_e32 v60, 1, v59
	v_cndmask_b32_e64 v56, v56, v2, s[12:13]
	v_cmp_eq_u32_e64 s[12:13], 1, v60
	s_or_b64 vcc, s[12:13], vcc
	v_cndmask_b32_e32 v52, v52, v143, vcc
	v_bitop3_b32 v60, v58, 2, v53 bitop3:0xc8
	v_cmp_eq_u32_e32 vcc, 0, v60
	v_cmp_gt_f32_e64 s[12:13], v34, v52
	s_and_b64 vcc, vcc, s[12:13]
	v_cndmask_b32_e32 v34, v52, v34, vcc
	v_bitop3_b32 v52, v58, 4, v53 bitop3:0xc8
	v_cndmask_b32_e64 v60, 0, 1, vcc
	v_cmp_eq_u32_e32 vcc, 0, v52
	v_cmp_gt_f32_e64 s[12:13], v33, v34
	s_and_b64 vcc, vcc, s[12:13]
	v_cndmask_b32_e32 v33, v34, v33, vcc
	v_bitop3_b32 v34, v58, 8, v53 bitop3:0xc8
	v_cndmask_b32_e64 v52, v60, 2, vcc
	v_cmp_eq_u32_e32 vcc, 0, v34
	v_cmp_gt_f32_e64 s[12:13], v32, v33
	s_and_b64 vcc, vcc, s[12:13]
	v_cndmask_b32_e32 v32, v33, v32, vcc
	v_bitop3_b32 v33, v58, 16, v53 bitop3:0xc8
	v_cndmask_b32_e64 v34, v52, 3, vcc
	v_cmp_eq_u32_e32 vcc, 0, v33
	v_cmp_gt_f32_e64 s[12:13], v31, v32
	s_and_b64 vcc, vcc, s[12:13]
	v_cndmask_b32_e32 v31, v32, v31, vcc
	v_bitop3_b32 v32, v58, 32, v53 bitop3:0xc8
	v_cndmask_b32_e64 v33, v34, 4, vcc
	v_cmp_eq_u32_e32 vcc, 0, v32
	v_cmp_gt_f32_e64 s[12:13], v30, v31
	s_and_b64 vcc, vcc, s[12:13]
	v_cndmask_b32_e32 v30, v31, v30, vcc
	v_bitop3_b32 v31, v58, 64, v53 bitop3:0xc8
	v_cndmask_b32_e64 v32, v33, 5, vcc
	v_cmp_eq_u32_e32 vcc, 0, v31
	v_cmp_gt_f32_e64 s[12:13], v29, v30
	s_and_b64 vcc, vcc, s[12:13]
	v_cndmask_b32_e32 v29, v30, v29, vcc
	v_bitop3_b32 v30, v58, s49, v53 bitop3:0xc8
	v_cndmask_b32_e64 v31, v32, 6, vcc
	v_cmp_eq_u32_e32 vcc, 0, v30
	v_cmp_gt_f32_e64 s[12:13], v28, v29
	s_and_b64 vcc, vcc, s[12:13]
	v_cndmask_b32_e32 v28, v29, v28, vcc
	v_bitop3_b32 v29, v58, s39, v53 bitop3:0xc8
	v_cndmask_b32_e64 v30, v31, 7, vcc
	v_cmp_eq_u32_e32 vcc, 0, v29
	v_cmp_gt_f32_e64 s[12:13], v27, v28
	s_and_b64 vcc, vcc, s[12:13]
	s_movk_i32 s12, 0x200
	v_cndmask_b32_e32 v27, v28, v27, vcc
	v_bitop3_b32 v28, v58, s12, v53 bitop3:0xc8
	v_cndmask_b32_e64 v29, v30, 8, vcc
	v_cmp_eq_u32_e32 vcc, 0, v28
	v_cmp_gt_f32_e64 s[12:13], v26, v27
	s_and_b64 vcc, vcc, s[12:13]
	s_movk_i32 s12, 0x400
	v_cndmask_b32_e32 v26, v27, v26, vcc
	v_bitop3_b32 v27, v58, s12, v53 bitop3:0xc8
	v_cndmask_b32_e64 v28, v29, 9, vcc
	v_cmp_eq_u32_e32 vcc, 0, v27
	v_cmp_gt_f32_e64 s[12:13], v25, v26
	s_and_b64 vcc, vcc, s[12:13]
	v_cndmask_b32_e32 v25, v26, v25, vcc
	v_bitop3_b32 v26, v58, s3, v53 bitop3:0xc8
	v_cndmask_b32_e64 v27, v28, 10, vcc
	v_cmp_eq_u32_e32 vcc, 0, v26
	v_cmp_gt_f32_e64 s[12:13], v24, v25
	s_and_b64 vcc, vcc, s[12:13]
	v_cndmask_b32_e32 v24, v25, v24, vcc
	v_bitop3_b32 v25, v58, s50, v53 bitop3:0xc8
	v_cndmask_b32_e64 v26, v27, 11, vcc
	v_cmp_eq_u32_e32 vcc, 0, v25
	v_cmp_gt_f32_e64 s[12:13], v23, v24
	s_and_b64 vcc, vcc, s[12:13]
	v_cndmask_b32_e32 v23, v24, v23, vcc
	v_bitop3_b32 v24, v58, s51, v53 bitop3:0xc8
	v_cndmask_b32_e64 v25, v26, 12, vcc
	v_cmp_eq_u32_e32 vcc, 0, v24
	v_cmp_gt_f32_e64 s[12:13], v22, v23
	s_and_b64 vcc, vcc, s[12:13]
	v_cndmask_b32_e32 v22, v23, v22, vcc
	v_bitop3_b32 v23, v58, s52, v53 bitop3:0xc8
	v_cndmask_b32_e64 v24, v25, 13, vcc
	v_cmp_eq_u32_e32 vcc, 0, v23
	v_cmp_gt_f32_e64 s[12:13], v21, v22
	s_and_b64 vcc, vcc, s[12:13]
	v_cndmask_b32_e32 v21, v22, v21, vcc
	v_bitop3_b32 v22, v58, s53, v53 bitop3:0xc8
	v_cndmask_b32_e64 v23, v24, 14, vcc
	v_cmp_eq_u32_e32 vcc, 0, v22
	v_cmp_gt_f32_e64 s[12:13], v20, v21
	s_and_b64 vcc, vcc, s[12:13]
	s_mov_b32 s12, 0x10000
	v_cndmask_b32_e32 v20, v21, v20, vcc
	v_bitop3_b32 v21, v58, s12, v53 bitop3:0xc8
	v_cndmask_b32_e64 v22, v23, 15, vcc
	v_cmp_eq_u32_e32 vcc, 0, v21
	v_cmp_gt_f32_e64 s[12:13], v18, v20
	s_and_b64 vcc, vcc, s[12:13]
	v_cndmask_b32_e32 v18, v20, v18, vcc
	v_bitop3_b32 v20, v58, s54, v53 bitop3:0xc8
	v_cndmask_b32_e64 v21, v22, 16, vcc
	v_cmp_eq_u32_e32 vcc, 0, v20
	v_cmp_gt_f32_e64 s[12:13], v17, v18
	s_and_b64 vcc, vcc, s[12:13]
	v_cndmask_b32_e32 v17, v18, v17, vcc
	v_bitop3_b32 v18, v58, s55, v53 bitop3:0xc8
	v_cndmask_b32_e64 v20, v21, 17, vcc
	v_cmp_eq_u32_e32 vcc, 0, v18
	v_cmp_gt_f32_e64 s[12:13], v16, v17
	s_and_b64 vcc, vcc, s[12:13]
	v_cndmask_b32_e32 v16, v17, v16, vcc
	v_bitop3_b32 v17, v58, s56, v53 bitop3:0xc8
	v_cndmask_b32_e64 v18, v20, 18, vcc
	v_cmp_eq_u32_e32 vcc, 0, v17
	v_cmp_gt_f32_e64 s[12:13], v15, v16
	s_and_b64 vcc, vcc, s[12:13]
	v_cndmask_b32_e32 v15, v16, v15, vcc
	v_bitop3_b32 v16, v58, s57, v53 bitop3:0xc8
	v_cndmask_b32_e64 v17, v18, 19, vcc
	v_cmp_eq_u32_e32 vcc, 0, v16
	v_cmp_gt_f32_e64 s[12:13], v14, v15
	s_and_b64 vcc, vcc, s[12:13]
	v_cndmask_b32_e32 v14, v15, v14, vcc
	v_bitop3_b32 v15, v58, s58, v53 bitop3:0xc8
	v_cndmask_b32_e64 v16, v17, 20, vcc
	v_cmp_eq_u32_e32 vcc, 0, v15
	v_cmp_gt_f32_e64 s[12:13], v13, v14
	s_and_b64 vcc, vcc, s[12:13]
	v_cndmask_b32_e32 v13, v14, v13, vcc
	v_bitop3_b32 v14, v58, s59, v53 bitop3:0xc8
	v_cndmask_b32_e64 v15, v16, 21, vcc
	v_cmp_eq_u32_e32 vcc, 0, v14
	v_cmp_gt_f32_e64 s[12:13], v11, v13
	s_and_b64 vcc, vcc, s[12:13]
	v_cndmask_b32_e32 v11, v13, v11, vcc
	v_bitop3_b32 v13, v58, s60, v53 bitop3:0xc8
	v_cndmask_b32_e64 v14, v15, 22, vcc
	v_cmp_eq_u32_e32 vcc, 0, v13
	v_cmp_gt_f32_e64 s[12:13], v10, v11
	s_and_b64 vcc, vcc, s[12:13]
	v_cndmask_b32_e32 v10, v11, v10, vcc
	v_bitop3_b32 v11, v58, s61, v53 bitop3:0xc8
	v_cndmask_b32_e64 v13, v14, 23, vcc
	v_cmp_eq_u32_e32 vcc, 0, v11
	v_cmp_gt_f32_e64 s[12:13], v9, v10
	s_and_b64 vcc, vcc, s[12:13]
	v_cndmask_b32_e32 v9, v10, v9, vcc
	v_bitop3_b32 v10, v58, s62, v53 bitop3:0xc8
	v_cndmask_b32_e64 v11, v13, 24, vcc
	v_cmp_eq_u32_e32 vcc, 0, v10
	v_cmp_gt_f32_e64 s[12:13], v8, v9
	s_and_b64 vcc, vcc, s[12:13]
	v_cndmask_b32_e32 v8, v9, v8, vcc
	v_bitop3_b32 v9, v58, s63, v53 bitop3:0xc8
	v_cndmask_b32_e64 v10, v11, 25, vcc
	v_cmp_eq_u32_e32 vcc, 0, v9
	v_cmp_gt_f32_e64 s[12:13], v7, v8
	s_and_b64 vcc, vcc, s[12:13]
	v_cndmask_b32_e32 v7, v8, v7, vcc
	v_bitop3_b32 v8, v58, s64, v53 bitop3:0xc8
	v_cndmask_b32_e64 v9, v10, 26, vcc
	v_cmp_eq_u32_e32 vcc, 0, v8
	v_cmp_gt_f32_e64 s[12:13], v6, v7
	s_and_b64 vcc, vcc, s[12:13]
	v_cndmask_b32_e32 v6, v7, v6, vcc
	v_bitop3_b32 v7, v58, s65, v53 bitop3:0xc8
	v_cndmask_b32_e64 v8, v9, 27, vcc
	v_cmp_eq_u32_e32 vcc, 0, v7
	v_cmp_gt_f32_e64 s[12:13], v5, v6
	s_and_b64 vcc, vcc, s[12:13]
	v_cndmask_b32_e32 v5, v6, v5, vcc
	v_bitop3_b32 v6, v58, s66, v53 bitop3:0xc8
	v_cndmask_b32_e64 v7, v8, 28, vcc
	v_cmp_eq_u32_e32 vcc, 0, v6
	v_cmp_gt_f32_e64 s[12:13], v4, v5
	s_and_b64 vcc, vcc, s[12:13]
	v_cndmask_b32_e32 v4, v5, v4, vcc
	v_bitop3_b32 v5, v58, 2.0, v53 bitop3:0xc8
	v_cndmask_b32_e64 v6, v7, 29, vcc
	v_cmp_eq_u32_e32 vcc, 0, v5
	v_cmp_gt_f32_e64 s[12:13], v3, v4
	s_and_b64 vcc, vcc, s[12:13]
	v_cndmask_b32_e32 v3, v4, v3, vcc
	v_cndmask_b32_e64 v5, v6, 30, vcc
	v_cmp_lt_i32_e32 vcc, -1, v59
	v_cmp_gt_f32_e64 s[12:13], v2, v3
	s_and_b64 vcc, vcc, s[12:13]
	v_cndmask_b32_e32 v2, v3, v2, vcc
	v_sub_f32_e32 v3, v54, v19
	v_cndmask_b32_e64 v4, v5, 31, vcc
	v_mul_f32_e32 v3, 0x3fb8aa3b, v3
	v_sub_f32_e32 v5, v56, v19
	v_exp_f32_e32 v3, v3
	v_mul_f32_e32 v5, 0x3fb8aa3b, v5
	v_sub_f32_e32 v2, v2, v19
	v_exp_f32_e32 v5, v5
	v_mul_f32_e32 v2, 0x3fb8aa3b, v2
	v_exp_f32_e32 v2, v2
	v_add_f32_e32 v6, 1.0, v3
	v_add_f32_e32 v6, v6, v5
	v_add_f32_e32 v6, v6, v2
	v_div_scale_f32 v7, s[12:13], v6, v6, 1.0
	v_rcp_f32_e32 v8, v7
	s_nop 0
	v_fma_f32 v9, -v7, v8, 1.0
	v_fmac_f32_e32 v8, v9, v8
	v_div_scale_f32 v9, vcc, 1.0, v6, 1.0
	v_mul_f32_e32 v10, v9, v8
	v_fma_f32 v11, -v7, v10, v9
	v_fmac_f32_e32 v10, v11, v8
	v_fma_f32 v7, -v7, v10, v9
	v_div_fmas_f32 v7, v7, v8, v10
	v_div_fixup_f32 v6, v7, v6, 1.0
	ds_write_b32 v116, v12
	ds_write_b32 v117, v6
	v_lshl_add_u32 v7, v12, 2, s38
	ds_add_rtn_u32 v7, v7, v142
	v_mul_f32_e32 v3, v3, v6
	s_waitcnt lgkmcnt(0)
	ds_write_b32 v118, v7
	ds_write_b32 v119, v55
	ds_write_b32 v120, v3
	v_lshl_add_u32 v3, v55, 2, s38
	ds_add_rtn_u32 v3, v3, v142
	v_mul_f32_e32 v5, v5, v6
	s_waitcnt lgkmcnt(0)
	ds_write_b32 v121, v3
	ds_write_b32 v122, v57
	ds_write_b32 v123, v5
	v_lshl_add_u32 v3, v57, 2, s38
	ds_add_rtn_u32 v3, v3, v142
	v_mul_f32_e32 v2, v2, v6
	s_waitcnt lgkmcnt(0)
	ds_write_b32 v124, v3
	ds_write_b32 v125, v4
	ds_write_b32 v126, v2
	v_lshl_add_u32 v2, v4, 2, s38
	ds_add_rtn_u32 v2, v2, v142
	s_waitcnt lgkmcnt(0)
	ds_write_b32 v127, v2
